# passL loop rewritten: coalesced 8-lane-per-row gathers, m1 staged via LDS to MFMA layout, prefetch; removed 64-bit division in passA/passL
# speedup vs baseline: 1.0412x; 1.0412x over previous
.LBB5_104:
	v_mov_b32_e32 v1, 0
	s_waitcnt vmcnt(0)
	v_lshl_add_u64 v[2:3], v[0:1], 2, s[14:15]
	global_store_dword v[2:3], v7, off offset:2048
	s_or_b64 exec, exec, s[0:1]
	s_and_saveexec_b64 s[0:1], s[4:5]
	s_cbranch_execnz .LBB5_83
	s_branch .LBB5_84
	.p2align	8

_Z7k_passAItEvPKiS1_PKfPKT_S6_S3_Pd:
	s_load_dwordx2 s[4:5], s[0:1], 0x28
	s_load_dword s6, s[0:1], 0x38
	v_lshlrev_b32_e32 v1, 3, v0
	v_and_b32_e32 v1, 56, v1
	v_lshlrev_b32_e32 v10, 2, v1
	s_waitcnt lgkmcnt(0)
	global_load_dwordx3 v[6:8], v10, s[4:5] offset:16
	global_load_dwordx4 v[2:5], v10, s[4:5]
	v_readfirstlane_b32 s3, v0
	s_lshl_b32 s7, s2, 2
	s_lshr_b32 s3, s3, 6
	s_add_i32 s16, s3, s7
	s_mul_i32 s14, s16, 0x7a12
	s_add_i32 s16, s14, 0x7a12
	s_lshr_b32 s14, s14, 12
	s_lshr_b32 s16, s16, 12
	v_mov_b32_e32 v11, 0

.LBB6_15:
	s_endpgm
	.p2align	8

.LBB7_2:
	s_or_b64 exec, exec, s[10:11]
	s_waitcnt lgkmcnt(0)
	s_barrier
	s_lshr_b32 s3, s3, 6
	s_lshl_b32 s5, s2, 2
	s_add_i32 s14, s3, s5
	s_mul_i32 s6, s14, 0x7a12
	s_add_i32 s10, s6, 0x7a12
	s_lshr_b32 s6, s6, 12
	s_lshr_b32 s10, s10, 12
.LBB7_8:
	s_load_dwordx2 s[12:13], s[0:1], 0x68
	s_lshl_b32 s17, s6, 5
	s_lshl_b32 s18, s10, 5
	s_sub_i32 s4, s18, s17
	s_ashr_i32 s16, s4, 5
	s_cmp_lt_i32 s16, 1
	v_and_b32_e32 v1, 63, v0
	s_cbranch_scc1 .LBB7_13
	s_load_dwordx8 s[4:11], s[0:1], 0x0
	s_load_dwordx2 s[14:15], s[0:1], 0x20
	v_and_b32_e32 v54, 7, v1
	v_lshlrev_b32_e32 v54, 4, v54
	v_lshrrev_b32_e32 v56, 3, v1
	v_lshlrev_b32_e32 v55, 1, v54
	ds_read_b128 v[2:5], v55 offset:18432
	ds_read_b128 v[6:9], v55 offset:18448
	ds_read_b128 v[10:13], v55 offset:18944
	ds_read_b128 v[14:17], v55 offset:18960
	ds_read_b128 v[18:21], v55 offset:18688
	ds_read_b128 v[22:25], v55 offset:18704
	s_mul_i32 s21, s3, 0x1200
	s_add_i32 s21, s21, 0x4b00
	v_mul_u32_u24_e32 v58, 0x240, v56
	v_add3_u32 v58, v58, v54, s21
	v_and_b32_e32 v59, 31, v1
	v_mul_u32_u24_e32 v59, 0x90, v59
	v_lshrrev_b32_e32 v57, 5, v1
	v_lshlrev_b32_e32 v57, 6, v57
	v_add3_u32 v59, v59, v57, s21
	v_lshlrev_b32_e32 v56, 4, v56
	v_lshlrev_b32_e32 v57, 4, v1
	v_mov_b32_e32 v50, 0
	v_mov_b32_e32 v51, 0
	v_mov_b32_e32 v52, 0
	v_mov_b32_e32 v53, 0
	s_lshl_b32 s20, s17, 2
	s_mov_b32 s22, 0x3d0880
	v_add_u32_e32 v55, s20, v56
	s_waitcnt lgkmcnt(0)
	global_load_dwordx4 v[26:29], v55, s[4:5]
	global_load_dwordx4 v[30:33], v55, s[6:7]
	global_load_dwordx4 v[34:37], v55, s[8:9]
	s_add_i32 s20, s20, 0x80
	s_min_u32 s23, s20, s22
	v_add_u32_e32 v55, s23, v56
	s_add_i32 s20, s20, 0x80
	s_waitcnt vmcnt(1)
	v_lshl_or_b32 v42, v30, 7, v54
	v_lshl_or_b32 v46, v26, 7, v54
	v_lshl_or_b32 v43, v31, 7, v54
	v_lshl_or_b32 v47, v27, 7, v54
	v_lshl_or_b32 v44, v32, 7, v54
	v_lshl_or_b32 v48, v28, 7, v54
	v_lshl_or_b32 v45, v33, 7, v54
	v_lshl_or_b32 v49, v29, 7, v54
	global_load_dwordx4 v[60:63], v42, s[10:11]
	global_load_dwordx4 v[76:79], v46, s[14:15]
	global_load_dwordx4 v[64:67], v43, s[10:11]
	global_load_dwordx4 v[80:83], v47, s[14:15]
	global_load_dwordx4 v[68:71], v44, s[10:11]
	global_load_dwordx4 v[84:87], v48, s[14:15]
	global_load_dwordx4 v[72:75], v45, s[10:11]
	global_load_dwordx4 v[88:91], v49, s[14:15]
	global_load_dwordx4 v[26:29], v55, s[4:5]
	global_load_dwordx4 v[30:33], v55, s[6:7]
	global_load_dwordx4 v[38:41], v55, s[8:9]
.Lpl_loop:
	s_waitcnt vmcnt(3)
	v_lshlrev_b32_e32 v92, 16, v60
	v_and_b32_e32 v93, 0xffff0000, v60
	v_lshlrev_b32_e32 v94, 16, v76
	v_and_b32_e32 v95, 0xffff0000, v76
	v_add_f32_e32 v92, v94, v92
	v_add_f32_e32 v93, v95, v93
	v_fma_f32 v94, v10, v34, v18
	v_fma_f32 v95, v11, v34, v19
	v_fmac_f32_e32 v94, v2, v92
	v_fmac_f32_e32 v95, v3, v93
	v_max_f32_e32 v94, 0, v94
	v_max_f32_e32 v95, 0, v95
	v_cvt_pk_f16_f32 v100, v94, v95
	v_lshlrev_b32_e32 v96, 16, v61
	v_and_b32_e32 v97, 0xffff0000, v61
	v_lshlrev_b32_e32 v98, 16, v77
	v_and_b32_e32 v99, 0xffff0000, v77
	v_add_f32_e32 v96, v98, v96
	v_add_f32_e32 v97, v99, v97
	v_fma_f32 v98, v12, v34, v20
	v_fma_f32 v99, v13, v34, v21
	v_fmac_f32_e32 v98, v4, v96
	v_fmac_f32_e32 v99, v5, v97
	v_max_f32_e32 v98, 0, v98
	v_max_f32_e32 v99, 0, v99
	v_cvt_pk_f16_f32 v101, v98, v99
	v_lshlrev_b32_e32 v92, 16, v62
	v_and_b32_e32 v93, 0xffff0000, v62
	v_lshlrev_b32_e32 v94, 16, v78
	v_and_b32_e32 v95, 0xffff0000, v78
	v_add_f32_e32 v92, v94, v92
	v_add_f32_e32 v93, v95, v93
	v_fma_f32 v94, v14, v34, v22
	v_fma_f32 v95, v15, v34, v23
	v_fmac_f32_e32 v94, v6, v92
	v_fmac_f32_e32 v95, v7, v93
	v_max_f32_e32 v94, 0, v94
	v_max_f32_e32 v95, 0, v95
	v_cvt_pk_f16_f32 v102, v94, v95
	v_lshlrev_b32_e32 v96, 16, v63
	v_and_b32_e32 v97, 0xffff0000, v63
	v_lshlrev_b32_e32 v98, 16, v79
	v_and_b32_e32 v99, 0xffff0000, v79
	v_add_f32_e32 v96, v98, v96
	v_add_f32_e32 v97, v99, v97
	v_fma_f32 v98, v16, v34, v24
	v_fma_f32 v99, v17, v34, v25
	v_fmac_f32_e32 v98, v8, v96
	v_fmac_f32_e32 v99, v9, v97
	v_max_f32_e32 v98, 0, v98
	v_max_f32_e32 v99, 0, v99
	v_cvt_pk_f16_f32 v103, v98, v99
	ds_write_b128 v58, v[100:103]
	v_lshlrev_b32_e32 v92, 16, v64
	v_and_b32_e32 v93, 0xffff0000, v64
	v_lshlrev_b32_e32 v94, 16, v80
	v_and_b32_e32 v95, 0xffff0000, v80
	v_add_f32_e32 v92, v94, v92
	v_add_f32_e32 v93, v95, v93
	v_fma_f32 v94, v10, v35, v18
	v_fma_f32 v95, v11, v35, v19
	v_fmac_f32_e32 v94, v2, v92
	v_fmac_f32_e32 v95, v3, v93
	v_max_f32_e32 v94, 0, v94
	v_max_f32_e32 v95, 0, v95
	v_cvt_pk_f16_f32 v104, v94, v95
	v_lshlrev_b32_e32 v96, 16, v65
	v_and_b32_e32 v97, 0xffff0000, v65
	v_lshlrev_b32_e32 v98, 16, v81
	v_and_b32_e32 v99, 0xffff0000, v81
	v_add_f32_e32 v96, v98, v96
	v_add_f32_e32 v97, v99, v97
	v_fma_f32 v98, v12, v35, v20
	v_fma_f32 v99, v13, v35, v21
	v_fmac_f32_e32 v98, v4, v96
	v_fmac_f32_e32 v99, v5, v97
	v_max_f32_e32 v98, 0, v98
	v_max_f32_e32 v99, 0, v99
	v_cvt_pk_f16_f32 v105, v98, v99
	v_lshlrev_b32_e32 v92, 16, v66
	v_and_b32_e32 v93, 0xffff0000, v66
	v_lshlrev_b32_e32 v94, 16, v82
	v_and_b32_e32 v95, 0xffff0000, v82
	v_add_f32_e32 v92, v94, v92
	v_add_f32_e32 v93, v95, v93
	v_fma_f32 v94, v14, v35, v22
	v_fma_f32 v95, v15, v35, v23
	v_fmac_f32_e32 v94, v6, v92
	v_fmac_f32_e32 v95, v7, v93
	v_max_f32_e32 v94, 0, v94
	v_max_f32_e32 v95, 0, v95
	v_cvt_pk_f16_f32 v106, v94, v95
	v_lshlrev_b32_e32 v96, 16, v67
	v_and_b32_e32 v97, 0xffff0000, v67
	v_lshlrev_b32_e32 v98, 16, v83
	v_and_b32_e32 v99, 0xffff0000, v83
	v_add_f32_e32 v96, v98, v96
	v_add_f32_e32 v97, v99, v97
	v_fma_f32 v98, v16, v35, v24
	v_fma_f32 v99, v17, v35, v25
	v_fmac_f32_e32 v98, v8, v96
	v_fmac_f32_e32 v99, v9, v97
	v_max_f32_e32 v98, 0, v98
	v_max_f32_e32 v99, 0, v99
	v_cvt_pk_f16_f32 v107, v98, v99
	ds_write_b128 v58, v[104:107] offset:144
	v_lshlrev_b32_e32 v92, 16, v68
	v_and_b32_e32 v93, 0xffff0000, v68
	v_lshlrev_b32_e32 v94, 16, v84
	v_and_b32_e32 v95, 0xffff0000, v84
	v_add_f32_e32 v92, v94, v92
	v_add_f32_e32 v93, v95, v93
	v_fma_f32 v94, v10, v36, v18
	v_fma_f32 v95, v11, v36, v19
	v_fmac_f32_e32 v94, v2, v92
	v_fmac_f32_e32 v95, v3, v93
	v_max_f32_e32 v94, 0, v94
	v_max_f32_e32 v95, 0, v95
	v_cvt_pk_f16_f32 v100, v94, v95
	v_lshlrev_b32_e32 v96, 16, v69
	v_and_b32_e32 v97, 0xffff0000, v69
	v_lshlrev_b32_e32 v98, 16, v85
	v_and_b32_e32 v99, 0xffff0000, v85
	v_add_f32_e32 v96, v98, v96
	v_add_f32_e32 v97, v99, v97
	v_fma_f32 v98, v12, v36, v20
	v_fma_f32 v99, v13, v36, v21
	v_fmac_f32_e32 v98, v4, v96
	v_fmac_f32_e32 v99, v5, v97
	v_max_f32_e32 v98, 0, v98
	v_max_f32_e32 v99, 0, v99
	v_cvt_pk_f16_f32 v101, v98, v99
	v_lshlrev_b32_e32 v92, 16, v70
	v_and_b32_e32 v93, 0xffff0000, v70
	v_lshlrev_b32_e32 v94, 16, v86
	v_and_b32_e32 v95, 0xffff0000, v86
	v_add_f32_e32 v92, v94, v92
	v_add_f32_e32 v93, v95, v93
	v_fma_f32 v94, v14, v36, v22
	v_fma_f32 v95, v15, v36, v23
	v_fmac_f32_e32 v94, v6, v92
	v_fmac_f32_e32 v95, v7, v93
	v_max_f32_e32 v94, 0, v94
	v_max_f32_e32 v95, 0, v95
	v_cvt_pk_f16_f32 v102, v94, v95
	v_lshlrev_b32_e32 v96, 16, v71
	v_and_b32_e32 v97, 0xffff0000, v71
	v_lshlrev_b32_e32 v98, 16, v87
	v_and_b32_e32 v99, 0xffff0000, v87
	v_add_f32_e32 v96, v98, v96
	v_add_f32_e32 v97, v99, v97
	v_fma_f32 v98, v16, v36, v24
	v_fma_f32 v99, v17, v36, v25
	v_fmac_f32_e32 v98, v8, v96
	v_fmac_f32_e32 v99, v9, v97
	v_max_f32_e32 v98, 0, v98
	v_max_f32_e32 v99, 0, v99
	v_cvt_pk_f16_f32 v103, v98, v99
	ds_write_b128 v58, v[100:103] offset:288
	v_lshlrev_b32_e32 v92, 16, v72
	v_and_b32_e32 v93, 0xffff0000, v72
	v_lshlrev_b32_e32 v94, 16, v88
	v_and_b32_e32 v95, 0xffff0000, v88
	v_add_f32_e32 v92, v94, v92
	v_add_f32_e32 v93, v95, v93
	v_fma_f32 v94, v10, v37, v18
	v_fma_f32 v95, v11, v37, v19
	v_fmac_f32_e32 v94, v2, v92
	v_fmac_f32_e32 v95, v3, v93
	v_max_f32_e32 v94, 0, v94
	v_max_f32_e32 v95, 0, v95
	v_cvt_pk_f16_f32 v104, v94, v95
	v_lshlrev_b32_e32 v96, 16, v73
	v_and_b32_e32 v97, 0xffff0000, v73
	v_lshlrev_b32_e32 v98, 16, v89
	v_and_b32_e32 v99, 0xffff0000, v89
	v_add_f32_e32 v96, v98, v96
	v_add_f32_e32 v97, v99, v97
	v_fma_f32 v98, v12, v37, v20
	v_fma_f32 v99, v13, v37, v21
	v_fmac_f32_e32 v98, v4, v96
	v_fmac_f32_e32 v99, v5, v97
	v_max_f32_e32 v98, 0, v98
	v_max_f32_e32 v99, 0, v99
	v_cvt_pk_f16_f32 v105, v98, v99
	v_lshlrev_b32_e32 v92, 16, v74
	v_and_b32_e32 v93, 0xffff0000, v74
	v_lshlrev_b32_e32 v94, 16, v90
	v_and_b32_e32 v95, 0xffff0000, v90
	v_add_f32_e32 v92, v94, v92
	v_add_f32_e32 v93, v95, v93
	v_fma_f32 v94, v14, v37, v22
	v_fma_f32 v95, v15, v37, v23
	v_fmac_f32_e32 v94, v6, v92
	v_fmac_f32_e32 v95, v7, v93
	v_max_f32_e32 v94, 0, v94
	v_max_f32_e32 v95, 0, v95
	v_cvt_pk_f16_f32 v106, v94, v95
	v_lshlrev_b32_e32 v96, 16, v75
	v_and_b32_e32 v97, 0xffff0000, v75
	v_lshlrev_b32_e32 v98, 16, v91
	v_and_b32_e32 v99, 0xffff0000, v91
	v_add_f32_e32 v96, v98, v96
	v_add_f32_e32 v97, v99, v97
	v_fma_f32 v98, v16, v37, v24
	v_fma_f32 v99, v17, v37, v25
	v_fmac_f32_e32 v98, v8, v96
	v_fmac_f32_e32 v99, v9, v97
	v_max_f32_e32 v98, 0, v98
	v_max_f32_e32 v99, 0, v99
	v_cvt_pk_f16_f32 v107, v98, v99
	ds_write_b128 v58, v[104:107] offset:432
	s_waitcnt vmcnt(0)
	v_lshl_or_b32 v42, v30, 7, v54
	v_lshl_or_b32 v46, v26, 7, v54
	v_lshl_or_b32 v43, v31, 7, v54
	v_lshl_or_b32 v47, v27, 7, v54
	v_lshl_or_b32 v44, v32, 7, v54
	v_lshl_or_b32 v48, v28, 7, v54
	v_lshl_or_b32 v45, v33, 7, v54
	v_lshl_or_b32 v49, v29, 7, v54
	global_load_dwordx4 v[60:63], v42, s[10:11]
	global_load_dwordx4 v[76:79], v46, s[14:15]
	global_load_dwordx4 v[64:67], v43, s[10:11]
	global_load_dwordx4 v[80:83], v47, s[14:15]
	global_load_dwordx4 v[68:71], v44, s[10:11]
	global_load_dwordx4 v[84:87], v48, s[14:15]
	global_load_dwordx4 v[72:75], v45, s[10:11]
	global_load_dwordx4 v[88:91], v49, s[14:15]
	v_mov_b32_e32 v34, v38
	v_mov_b32_e32 v35, v39
	v_mov_b32_e32 v36, v40
	v_mov_b32_e32 v37, v41
	s_min_u32 s23, s20, s22
	v_add_u32_e32 v55, s23, v56
	s_add_i32 s20, s20, 0x80
	global_load_dwordx4 v[26:29], v55, s[4:5]
	global_load_dwordx4 v[30:33], v55, s[6:7]
	global_load_dwordx4 v[38:41], v55, s[8:9]
	s_waitcnt lgkmcnt(0)
	ds_read_b128 v[92:95], v59
	ds_read_b128 v[96:99], v59 offset:16
	ds_read_b128 v[100:103], v59 offset:32
	ds_read_b128 v[104:107], v59 offset:48
	ds_read_b128 v[42:45], v57
	ds_read_b128 v[46:49], v57 offset:1024
	ds_read_b128 v[124:127], v57 offset:2048
	s_waitcnt lgkmcnt(2)
	v_mfma_f32_32x32x16_f16 v[108:123], v[92:95], v[42:45], 0
	ds_read_b128 v[42:45], v57 offset:3072
	s_waitcnt lgkmcnt(2)
	v_mfma_f32_32x32x16_f16 v[108:123], v[96:99], v[46:49], v[108:123]
	ds_read_b128 v[46:49], v57 offset:4096
	s_waitcnt lgkmcnt(2)
	v_mfma_f32_32x32x16_f16 v[108:123], v[100:103], v[124:127], v[108:123]
	ds_read_b128 v[124:127], v57 offset:5120
	s_waitcnt lgkmcnt(2)
	v_mfma_f32_32x32x16_f16 v[108:123], v[104:107], v[42:45], v[108:123]
	ds_read_b128 v[42:45], v57 offset:6144
	s_nop 11
	v_add_f32_e32 v52, v108, v52
	v_fmac_f32_e32 v50, v108, v108
	v_add_f32_e32 v52, v109, v52
	v_fmac_f32_e32 v50, v109, v109
	v_add_f32_e32 v52, v110, v52
	v_fmac_f32_e32 v50, v110, v110
	v_add_f32_e32 v52, v111, v52
	v_fmac_f32_e32 v50, v111, v111
	v_add_f32_e32 v52, v112, v52
	v_fmac_f32_e32 v50, v112, v112
	v_add_f32_e32 v52, v113, v52
	v_fmac_f32_e32 v50, v113, v113
	v_add_f32_e32 v52, v114, v52
	v_fmac_f32_e32 v50, v114, v114
	v_add_f32_e32 v52, v115, v52
	v_fmac_f32_e32 v50, v115, v115
	v_add_f32_e32 v52, v116, v52
	v_fmac_f32_e32 v50, v116, v116
	v_add_f32_e32 v52, v117, v52
	v_fmac_f32_e32 v50, v117, v117
	v_add_f32_e32 v52, v118, v52
	v_fmac_f32_e32 v50, v118, v118
	v_add_f32_e32 v52, v119, v52
	v_fmac_f32_e32 v50, v119, v119
	v_add_f32_e32 v52, v120, v52
	v_fmac_f32_e32 v50, v120, v120
	v_add_f32_e32 v52, v121, v52
	v_fmac_f32_e32 v50, v121, v121
	v_add_f32_e32 v52, v122, v52
	v_fmac_f32_e32 v50, v122, v122
	v_add_f32_e32 v52, v123, v52
	v_fmac_f32_e32 v50, v123, v123
	s_waitcnt lgkmcnt(2)
	v_mfma_f32_32x32x16_f16 v[108:123], v[92:95], v[46:49], 0
	ds_read_b128 v[46:49], v57 offset:7168
	s_waitcnt lgkmcnt(2)
	v_mfma_f32_32x32x16_f16 v[108:123], v[96:99], v[124:127], v[108:123]
	s_waitcnt lgkmcnt(1)
	v_mfma_f32_32x32x16_f16 v[108:123], v[100:103], v[42:45], v[108:123]
	s_waitcnt lgkmcnt(0)
	v_mfma_f32_32x32x16_f16 v[108:123], v[104:107], v[46:49], v[108:123]
	s_nop 11
	v_add_f32_e32 v53, v108, v53
	v_fmac_f32_e32 v51, v108, v108
	v_add_f32_e32 v53, v109, v53
	v_fmac_f32_e32 v51, v109, v109
	v_add_f32_e32 v53, v110, v53
	v_fmac_f32_e32 v51, v110, v110
	v_add_f32_e32 v53, v111, v53
	v_fmac_f32_e32 v51, v111, v111
	v_add_f32_e32 v53, v112, v53
	v_fmac_f32_e32 v51, v112, v112
	v_add_f32_e32 v53, v113, v53
	v_fmac_f32_e32 v51, v113, v113
	v_add_f32_e32 v53, v114, v53
	v_fmac_f32_e32 v51, v114, v114
	v_add_f32_e32 v53, v115, v53
	v_fmac_f32_e32 v51, v115, v115
	v_add_f32_e32 v53, v116, v53
	v_fmac_f32_e32 v51, v116, v116
	v_add_f32_e32 v53, v117, v53
	v_fmac_f32_e32 v51, v117, v117
	v_add_f32_e32 v53, v118, v53
	v_fmac_f32_e32 v51, v118, v118
	v_add_f32_e32 v53, v119, v53
	v_fmac_f32_e32 v51, v119, v119
	v_add_f32_e32 v53, v120, v53
	v_fmac_f32_e32 v51, v120, v120
	v_add_f32_e32 v53, v121, v53
	v_fmac_f32_e32 v51, v121, v121
	v_add_f32_e32 v53, v122, v53
	v_fmac_f32_e32 v51, v122, v122
	v_add_f32_e32 v53, v123, v53
	v_fmac_f32_e32 v51, v123, v123
	s_add_i32 s16, s16, -1
	s_cmp_lg_u32 s16, 0
	s_cbranch_scc1 .Lpl_loop
	s_branch .LBB7_14

	.amdhsa_kernel _Z7k_passLILi1ELi0ELi1EEvPKiS1_PKfPKtS5_S3_S3_S3_S3_S3_S3_PK15HIP_vector_typeIjLj4EEPKdPdS1_PtS1_
		.amdhsa_group_segment_fixed_size 37632
		.amdhsa_private_segment_fixed_size 0
		.amdhsa_kernarg_size 392
		.amdhsa_user_sgpr_count 2
		.amdhsa_user_sgpr_dispatch_ptr 0
		.amdhsa_user_sgpr_queue_ptr 0
		.amdhsa_user_sgpr_kernarg_segment_ptr 1
		.amdhsa_user_sgpr_dispatch_id 0
		.amdhsa_user_sgpr_kernarg_preload_length 0
		.amdhsa_user_sgpr_kernarg_preload_offset 0
		.amdhsa_user_sgpr_private_segment_size 0
		.amdhsa_uses_dynamic_stack 0
		.amdhsa_enable_private_segment 0
		.amdhsa_system_sgpr_workgroup_id_x 1
		.amdhsa_system_sgpr_workgroup_id_y 0
		.amdhsa_system_sgpr_workgroup_id_z 0
		.amdhsa_system_sgpr_workgroup_info 0
		.amdhsa_system_vgpr_workitem_id 0
		.amdhsa_next_free_vgpr 128
		.amdhsa_next_free_sgpr 28
		.amdhsa_accum_offset 128
		.amdhsa_reserve_vcc 1
		.amdhsa_float_round_mode_32 0
		.amdhsa_float_round_mode_16_64 0
		.amdhsa_float_denorm_mode_32 3
		.amdhsa_float_denorm_mode_16_64 3
		.amdhsa_dx10_clamp 1
		.amdhsa_ieee_mode 1
		.amdhsa_fp16_overflow 0
		.amdhsa_tg_split 0
		.amdhsa_exception_fp_ieee_invalid_op 0
		.amdhsa_exception_fp_denorm_src 0
		.amdhsa_exception_fp_ieee_div_zero 0
		.amdhsa_exception_fp_ieee_overflow 0
		.amdhsa_exception_fp_ieee_underflow 0
		.amdhsa_exception_fp_ieee_inexact 0
		.amdhsa_exception_int_div_zero 0
	.end_amdhsa_kernel

	.text
	.p2alignl 6, 3212836864
	.fill 256, 4, 3212836864
	.p2align	8

amdhsa.kernels:
  - .agpr_count:     0
    .args:
      - .actual_access:  read_only
        .address_space:  global
        .offset:         0
        .size:           8
        .value_kind:     global_buffer
      - .actual_access:  read_only
        .address_space:  global
        .offset:         8
        .size:           8
        .value_kind:     global_buffer
      - .actual_access:  read_only
        .address_space:  global
        .offset:         16
        .size:           8
        .value_kind:     global_buffer
      - .actual_access:  read_only
        .address_space:  global
        .offset:         24
        .size:           8
        .value_kind:     global_buffer
      - .actual_access:  write_only
        .address_space:  global
        .offset:         32
        .size:           8
        .value_kind:     global_buffer
      - .actual_access:  write_only
        .address_space:  global
        .offset:         40
        .size:           8
        .value_kind:     global_buffer
      - .actual_access:  write_only
        .address_space:  global
        .offset:         48
        .size:           8
        .value_kind:     global_buffer
      - .offset:         56
        .size:           4
        .value_kind:     hidden_block_count_x
      - .offset:         60
        .size:           4
        .value_kind:     hidden_block_count_y
      - .offset:         64
        .size:           4
        .value_kind:     hidden_block_count_z
      - .offset:         68
        .size:           2
        .value_kind:     hidden_group_size_x
      - .offset:         70
        .size:           2
        .value_kind:     hidden_group_size_y
      - .offset:         72
        .size:           2
        .value_kind:     hidden_group_size_z
      - .offset:         74
        .size:           2
        .value_kind:     hidden_remainder_x
      - .offset:         76
        .size:           2
        .value_kind:     hidden_remainder_y
      - .offset:         78
        .size:           2
        .value_kind:     hidden_remainder_z
      - .offset:         96
        .size:           8
        .value_kind:     hidden_global_offset_x
      - .offset:         104
        .size:           8
        .value_kind:     hidden_global_offset_y
      - .offset:         112
        .size:           8
        .value_kind:     hidden_global_offset_z
      - .offset:         120
        .size:           2
        .value_kind:     hidden_grid_dims
    .group_segment_fixed_size: 0
    .kernarg_segment_align: 8
    .kernarg_segment_size: 312
    .language:       OpenCL C
    .language_version:
      - 2
      - 0
    .max_flat_workgroup_size: 256
    .name:           _Z6k_prepPKfS0_S0_S0_P15HIP_vector_typeIjLj4EEPiPd
    .private_segment_fixed_size: 0
    .sgpr_count:     25
    .sgpr_spill_count: 0
    .symbol:         _Z6k_prepPKfS0_S0_S0_P15HIP_vector_typeIjLj4EEPiPd.kd
    .uniform_work_group_size: 1
    .uses_dynamic_stack: false
    .vgpr_count:     24
    .vgpr_spill_count: 0
    .wavefront_size: 64
  - .agpr_count:     0
    .args:
      - .actual_access:  read_only
        .address_space:  global
        .offset:         0
        .size:           8
        .value_kind:     global_buffer
      - .actual_access:  read_only
        .address_space:  global
        .offset:         8
        .size:           8
        .value_kind:     global_buffer
      - .actual_access:  read_only
        .address_space:  global
        .offset:         16
        .size:           8
        .value_kind:     global_buffer
      - .actual_access:  read_only
        .address_space:  global
        .offset:         24
        .size:           8
        .value_kind:     global_buffer
      - .actual_access:  read_only
        .address_space:  global
        .offset:         32
        .size:           8
        .value_kind:     global_buffer
      - .actual_access:  write_only
        .address_space:  global
        .offset:         40
        .size:           8
        .value_kind:     global_buffer
      - .actual_access:  write_only
        .address_space:  global
        .offset:         48
        .size:           8
        .value_kind:     global_buffer
    .group_segment_fixed_size: 4112
    .kernarg_segment_align: 8
    .kernarg_segment_size: 56
    .language:       OpenCL C
    .language_version:
      - 2
      - 0
    .max_flat_workgroup_size: 256
    .name:           _Z10k_bscatterPKiS0_PKfS0_S0_PiP15HIP_vector_typeIjLj2EE
    .private_segment_fixed_size: 0
    .sgpr_count:     28
    .sgpr_spill_count: 0
    .symbol:         _Z10k_bscatterPKiS0_PKfS0_S0_PiP15HIP_vector_typeIjLj2EE.kd
    .uniform_work_group_size: 1
    .uses_dynamic_stack: false
    .vgpr_count:     78
    .vgpr_spill_count: 0
    .wavefront_size: 64
  - .agpr_count:     0
    .args:
      - .actual_access:  read_only
        .address_space:  global
        .offset:         0
        .size:           8
        .value_kind:     global_buffer
      - .actual_access:  read_only
        .address_space:  global
        .offset:         8
        .size:           8
        .value_kind:     global_buffer
      - .actual_access:  write_only
        .address_space:  global
        .offset:         16
        .size:           8
        .value_kind:     global_buffer
      - .actual_access:  write_only
        .address_space:  global
        .offset:         24
        .size:           8
        .value_kind:     global_buffer
      - .actual_access:  write_only
        .address_space:  global
        .offset:         32
        .size:           8
        .value_kind:     global_buffer
      - .actual_access:  write_only
        .address_space:  global
        .offset:         40
        .size:           8
        .value_kind:     global_buffer
    .group_segment_fixed_size: 29200
    .kernarg_segment_align: 8
    .kernarg_segment_size: 48
    .language:       OpenCL C
    .language_version:
      - 2
      - 0
    .max_flat_workgroup_size: 256
    .name:           _Z7k_bsortPKiPK15HIP_vector_typeIjLj2EEPiS5_S5_Pf
    .private_segment_fixed_size: 0
    .sgpr_count:     106
    .sgpr_spill_count: 12
    .symbol:         _Z7k_bsortPKiPK15HIP_vector_typeIjLj2EEPiS5_S5_Pf.kd
    .uniform_work_group_size: 1
    .uses_dynamic_stack: false
    .vgpr_count:     69
    .vgpr_spill_count: 0
    .wavefront_size: 64
  - .agpr_count:     32
    .args:
      - .address_space:  global
        .offset:         0
        .size:           8
        .value_kind:     global_buffer
      - .actual_access:  read_only
        .address_space:  global
        .offset:         8
        .size:           8
        .value_kind:     global_buffer
      - .actual_access:  read_only
        .address_space:  global
        .offset:         16
        .size:           8
        .value_kind:     global_buffer
      - .actual_access:  read_only
        .address_space:  global
        .offset:         24
        .size:           8
        .value_kind:     global_buffer
      - .actual_access:  read_only
        .address_space:  global
        .offset:         32
        .size:           8
        .value_kind:     global_buffer
      - .actual_access:  read_only
        .address_space:  global
        .offset:         40
        .size:           8
        .value_kind:     global_buffer
      - .address_space:  global
        .offset:         48
        .size:           8
        .value_kind:     global_buffer
      - .address_space:  global
        .offset:         56
        .size:           8
        .value_kind:     global_buffer
      - .offset:         64
        .size:           4
        .value_kind:     hidden_block_count_x
      - .offset:         68
        .size:           4
        .value_kind:     hidden_block_count_y
      - .offset:         72
        .size:           4
        .value_kind:     hidden_block_count_z
      - .offset:         76
        .size:           2
        .value_kind:     hidden_group_size_x
      - .offset:         78
        .size:           2
        .value_kind:     hidden_group_size_y
      - .offset:         80
        .size:           2
        .value_kind:     hidden_group_size_z
      - .offset:         82
        .size:           2
        .value_kind:     hidden_remainder_x
      - .offset:         84
        .size:           2
        .value_kind:     hidden_remainder_y
      - .offset:         86
        .size:           2
        .value_kind:     hidden_remainder_z
      - .offset:         104
        .size:           8
        .value_kind:     hidden_global_offset_x
      - .offset:         112
        .size:           8
        .value_kind:     hidden_global_offset_y
      - .offset:         120
        .size:           8
        .value_kind:     hidden_global_offset_z
      - .offset:         128
        .size:           2
        .value_kind:     hidden_grid_dims
    .group_segment_fixed_size: 18944
    .kernarg_segment_align: 8
    .kernarg_segment_size: 320
    .language:       OpenCL C
    .language_version:
      - 2
      - 0
    .max_flat_workgroup_size: 256
    .name:           _Z4k_U2PKtPK15HIP_vector_typeIjLj4EEPKdPKfS8_S8_PtPd
    .private_segment_fixed_size: 0
    .sgpr_count:     20
    .sgpr_spill_count: 0
    .symbol:         _Z4k_U2PKtPK15HIP_vector_typeIjLj4EEPKdPKfS8_S8_PtPd.kd
    .uniform_work_group_size: 1
    .uses_dynamic_stack: false
    .vgpr_count:     104
    .vgpr_spill_count: 0
    .wavefront_size: 64
  - .agpr_count:     0
    .args:
      - .actual_access:  read_only
        .address_space:  global
        .offset:         0
        .size:           8
        .value_kind:     global_buffer
      - .actual_access:  read_only
        .address_space:  global
        .offset:         8
        .size:           8
        .value_kind:     global_buffer
      - .actual_access:  write_only
        .address_space:  global
        .offset:         16
        .size:           8
        .value_kind:     global_buffer
    .group_segment_fixed_size: 0
    .kernarg_segment_align: 8
    .kernarg_segment_size: 24
    .language:       OpenCL C
    .language_version:
      - 2
      - 0
    .max_flat_workgroup_size: 1024
    .name:           _Z7k_finalPKdPKfPf
    .private_segment_fixed_size: 0
    .sgpr_count:     28
    .sgpr_spill_count: 0
    .symbol:         _Z7k_finalPKdPKfPf.kd
    .uniform_work_group_size: 1
    .uses_dynamic_stack: false
    .vgpr_count:     10
    .vgpr_spill_count: 0
    .wavefront_size: 64
  - .agpr_count:     64
    .args:
      - .actual_access:  read_only
        .address_space:  global
        .offset:         0
        .size:           8
        .value_kind:     global_buffer
      - .address_space:  global
        .offset:         8
        .size:           8
        .value_kind:     global_buffer
      - .actual_access:  write_only
        .address_space:  global
        .offset:         16
        .size:           8
        .value_kind:     global_buffer
      - .actual_access:  read_only
        .address_space:  global
        .offset:         24
        .size:           8
        .value_kind:     global_buffer
      - .actual_access:  read_only
        .address_space:  global
        .offset:         32
        .size:           8
        .value_kind:     global_buffer
      - .actual_access:  read_only
        .address_space:  global
        .offset:         40
        .size:           8
        .value_kind:     global_buffer
      - .actual_access:  read_only
        .address_space:  global
        .offset:         48
        .size:           8
        .value_kind:     global_buffer
      - .actual_access:  read_only
        .address_space:  global
        .offset:         56
        .size:           8
        .value_kind:     global_buffer
      - .actual_access:  write_only
        .address_space:  global
        .offset:         64
        .size:           8
        .value_kind:     global_buffer
      - .actual_access:  write_only
        .address_space:  global
        .offset:         72
        .size:           8
        .value_kind:     global_buffer
      - .actual_access:  write_only
        .address_space:  global
        .offset:         80
        .size:           8
        .value_kind:     global_buffer
      - .offset:         88
        .size:           4
        .value_kind:     hidden_block_count_x
      - .offset:         92
        .size:           4
        .value_kind:     hidden_block_count_y
      - .offset:         96
        .size:           4
        .value_kind:     hidden_block_count_z
      - .offset:         100
        .size:           2
        .value_kind:     hidden_group_size_x
      - .offset:         102
        .size:           2
        .value_kind:     hidden_group_size_y
      - .offset:         104
        .size:           2
        .value_kind:     hidden_group_size_z
      - .offset:         106
        .size:           2
        .value_kind:     hidden_remainder_x
      - .offset:         108
        .size:           2
        .value_kind:     hidden_remainder_y
      - .offset:         110
        .size:           2
        .value_kind:     hidden_remainder_z
      - .offset:         128
        .size:           8
        .value_kind:     hidden_global_offset_x
      - .offset:         136
        .size:           8
        .value_kind:     hidden_global_offset_y
      - .offset:         144
        .size:           8
        .value_kind:     hidden_global_offset_z
      - .offset:         152
        .size:           2
        .value_kind:     hidden_grid_dims
    .group_segment_fixed_size: 45312
    .kernarg_segment_align: 8
    .kernarg_segment_size: 344
    .language:       OpenCL C
    .language_version:
      - 2
      - 0
    .max_flat_workgroup_size: 256
    .name:           _Z14k_bcount_node0ItEvPKiPiS2_PKfS4_S4_S4_PK15HIP_vector_typeIjLj4EEPtPT_SB_
    .private_segment_fixed_size: 0
    .sgpr_count:     26
    .sgpr_spill_count: 0
    .symbol:         _Z14k_bcount_node0ItEvPKiPiS2_PKfS4_S4_S4_PK15HIP_vector_typeIjLj4EEPtPT_SB_.kd
    .uniform_work_group_size: 1
    .uses_dynamic_stack: false
    .vgpr_count:     232
    .vgpr_spill_count: 0
    .wavefront_size: 64
  - .agpr_count:     0
    .args:
      - .actual_access:  read_only
        .address_space:  global
        .offset:         0
        .size:           8
        .value_kind:     global_buffer
      - .actual_access:  read_only
        .address_space:  global
        .offset:         8
        .size:           8
        .value_kind:     global_buffer
      - .actual_access:  read_only
        .address_space:  global
        .offset:         16
        .size:           8
        .value_kind:     global_buffer
      - .actual_access:  read_only
        .address_space:  global
        .offset:         24
        .size:           8
        .value_kind:     global_buffer
      - .actual_access:  read_only
        .address_space:  global
        .offset:         32
        .size:           8
        .value_kind:     global_buffer
      - .actual_access:  read_only
        .address_space:  global
        .offset:         40
        .size:           8
        .value_kind:     global_buffer
      - .address_space:  global
        .offset:         48
        .size:           8
        .value_kind:     global_buffer
      - .offset:         56
        .size:           4
        .value_kind:     hidden_block_count_x
      - .offset:         60
        .size:           4
        .value_kind:     hidden_block_count_y
      - .offset:         64
        .size:           4
        .value_kind:     hidden_block_count_z
      - .offset:         68
        .size:           2
        .value_kind:     hidden_group_size_x
      - .offset:         70
        .size:           2
        .value_kind:     hidden_group_size_y
      - .offset:         72
        .size:           2
        .value_kind:     hidden_group_size_z
      - .offset:         74
        .size:           2
        .value_kind:     hidden_remainder_x
      - .offset:         76
        .size:           2
        .value_kind:     hidden_remainder_y
      - .offset:         78
        .size:           2
        .value_kind:     hidden_remainder_z
      - .offset:         96
        .size:           8
        .value_kind:     hidden_global_offset_x
      - .offset:         104
        .size:           8
        .value_kind:     hidden_global_offset_y
      - .offset:         112
        .size:           8
        .value_kind:     hidden_global_offset_z
      - .offset:         120
        .size:           2
        .value_kind:     hidden_grid_dims
    .group_segment_fixed_size: 2048
    .kernarg_segment_align: 8
    .kernarg_segment_size: 312
    .language:       OpenCL C
    .language_version:
      - 2
      - 0
    .max_flat_workgroup_size: 256
    .name:           _Z7k_passAItEvPKiS1_PKfPKT_S6_S3_Pd
    .private_segment_fixed_size: 0
    .sgpr_count:     36
    .sgpr_spill_count: 0
    .symbol:         _Z7k_passAItEvPKiS1_PKfPKT_S6_S3_Pd.kd
    .uniform_work_group_size: 1
    .uses_dynamic_stack: false
    .vgpr_count:     104
    .vgpr_spill_count: 0
    .wavefront_size: 64
  - .agpr_count:     0
    .args:
      - .actual_access:  read_only
        .address_space:  global
        .offset:         0
        .size:           8
        .value_kind:     global_buffer
      - .actual_access:  read_only
        .address_space:  global
        .offset:         8
        .size:           8
        .value_kind:     global_buffer
      - .actual_access:  read_only
        .address_space:  global
        .offset:         16
        .size:           8
        .value_kind:     global_buffer
      - .actual_access:  read_only
        .address_space:  global
        .offset:         24
        .size:           8
        .value_kind:     global_buffer
      - .actual_access:  read_only
        .address_space:  global
        .offset:         32
        .size:           8
        .value_kind:     global_buffer
      - .actual_access:  read_only
        .address_space:  global
        .offset:         40
        .size:           8
        .value_kind:     global_buffer
      - .actual_access:  read_only
        .address_space:  global
        .offset:         48
        .size:           8
        .value_kind:     global_buffer
      - .actual_access:  read_only
        .address_space:  global
        .offset:         56
        .size:           8
        .value_kind:     global_buffer
      - .actual_access:  read_only
        .address_space:  global
        .offset:         64
        .size:           8
        .value_kind:     global_buffer
      - .actual_access:  read_only
        .address_space:  global
        .offset:         72
        .size:           8
        .value_kind:     global_buffer
      - .actual_access:  read_only
        .address_space:  global
        .offset:         80
        .size:           8
        .value_kind:     global_buffer
      - .actual_access:  read_only
        .address_space:  global
        .offset:         88
        .size:           8
        .value_kind:     global_buffer
      - .actual_access:  read_only
        .address_space:  global
        .offset:         96
        .size:           8
        .value_kind:     global_buffer
      - .address_space:  global
        .offset:         104
        .size:           8
        .value_kind:     global_buffer
      - .actual_access:  read_only
        .address_space:  global
        .offset:         112
        .size:           8
        .value_kind:     global_buffer
      - .actual_access:  read_only
        .address_space:  global
        .offset:         120
        .size:           8
        .value_kind:     global_buffer
      - .address_space:  global
        .offset:         128
        .size:           8
        .value_kind:     global_buffer
      - .offset:         136
        .size:           4
        .value_kind:     hidden_block_count_x
      - .offset:         140
        .size:           4
        .value_kind:     hidden_block_count_y
      - .offset:         144
        .size:           4
        .value_kind:     hidden_block_count_z
      - .offset:         148
        .size:           2
        .value_kind:     hidden_group_size_x
      - .offset:         150
        .size:           2
        .value_kind:     hidden_group_size_y
      - .offset:         152
        .size:           2
        .value_kind:     hidden_group_size_z
      - .offset:         154
        .size:           2
        .value_kind:     hidden_remainder_x
      - .offset:         156
        .size:           2
        .value_kind:     hidden_remainder_y
      - .offset:         158
        .size:           2
        .value_kind:     hidden_remainder_z
      - .offset:         176
        .size:           8
        .value_kind:     hidden_global_offset_x
      - .offset:         184
        .size:           8
        .value_kind:     hidden_global_offset_y
      - .offset:         192
        .size:           8
        .value_kind:     hidden_global_offset_z
      - .offset:         200
        .size:           2
        .value_kind:     hidden_grid_dims
    .group_segment_fixed_size: 37632
    .kernarg_segment_align: 8
    .kernarg_segment_size: 392
    .language:       OpenCL C
    .language_version:
      - 2
      - 0
    .max_flat_workgroup_size: 256
    .name:           _Z7k_passLILi1ELi0ELi1EEvPKiS1_PKfPKtS5_S3_S3_S3_S3_S3_S3_PK15HIP_vector_typeIjLj4EEPKdPdS1_PtS1_
    .private_segment_fixed_size: 0
    .sgpr_count:     34
    .sgpr_spill_count: 0
    .symbol:         _Z7k_passLILi1ELi0ELi1EEvPKiS1_PKfPKtS5_S3_S3_S3_S3_S3_S3_PK15HIP_vector_typeIjLj4EEPKdPdS1_PtS1_.kd
    .uniform_work_group_size: 1
    .uses_dynamic_stack: false
    .vgpr_count:     128
    .vgpr_spill_count: 0
    .wavefront_size: 64
  - .agpr_count:     0
    .args:
      - .actual_access:  read_only
        .address_space:  global
        .offset:         0
        .size:           8
        .value_kind:     global_buffer
      - .actual_access:  read_only
        .address_space:  global
        .offset:         8
        .size:           8
        .value_kind:     global_buffer
      - .actual_access:  read_only
        .address_space:  global
        .offset:         16
        .size:           8
        .value_kind:     global_buffer
      - .actual_access:  read_only
        .address_space:  global
        .offset:         24
        .size:           8
        .value_kind:     global_buffer
      - .actual_access:  read_only
        .address_space:  global
        .offset:         32
        .size:           8
        .value_kind:     global_buffer
      - .actual_access:  read_only
        .address_space:  global
        .offset:         40
        .size:           8
        .value_kind:     global_buffer
      - .actual_access:  read_only
        .address_space:  global
        .offset:         48
        .size:           8
        .value_kind:     global_buffer
      - .actual_access:  read_only
        .address_space:  global
        .offset:         56
        .size:           8
        .value_kind:     global_buffer
      - .actual_access:  read_only
        .address_space:  global
        .offset:         64
        .size:           8
        .value_kind:     global_buffer
      - .actual_access:  read_only
        .address_space:  global
        .offset:         72
        .size:           8
        .value_kind:     global_buffer
      - .actual_access:  read_only
        .address_space:  global
        .offset:         80
        .size:           8
        .value_kind:     global_buffer
      - .actual_access:  read_only
        .address_space:  global
        .offset:         88
        .size:           8
        .value_kind:     global_buffer
      - .actual_access:  read_only
        .address_space:  global
        .offset:         96
        .size:           8
        .value_kind:     global_buffer
      - .actual_access:  read_only
        .address_space:  global
        .offset:         104
        .size:           8
        .value_kind:     global_buffer
      - .actual_access:  read_only
        .address_space:  global
        .offset:         112
        .size:           8
        .value_kind:     global_buffer
      - .actual_access:  read_only
        .address_space:  global
        .offset:         120
        .size:           8
        .value_kind:     global_buffer
      - .actual_access:  read_only
        .address_space:  global
        .offset:         128
        .size:           8
        .value_kind:     global_buffer
      - .address_space:  global
        .offset:         136
        .size:           8
        .value_kind:     global_buffer
      - .actual_access:  read_only
        .address_space:  global
        .offset:         144
        .size:           8
        .value_kind:     global_buffer
      - .actual_access:  read_only
        .address_space:  global
        .offset:         152
        .size:           8
        .value_kind:     global_buffer
      - .actual_access:  write_only
        .address_space:  global
        .offset:         160
        .size:           8
        .value_kind:     global_buffer
      - .address_space:  global
        .offset:         168
        .size:           8
        .value_kind:     global_buffer
      - .offset:         176
        .size:           4
        .value_kind:     hidden_block_count_x
      - .offset:         180
        .size:           4
        .value_kind:     hidden_block_count_y
      - .offset:         184
        .size:           4
        .value_kind:     hidden_block_count_z
      - .offset:         188
        .size:           2
        .value_kind:     hidden_group_size_x
      - .offset:         190
        .size:           2
        .value_kind:     hidden_group_size_y
      - .offset:         192
        .size:           2
        .value_kind:     hidden_group_size_z
      - .offset:         194
        .size:           2
        .value_kind:     hidden_remainder_x
      - .offset:         196
        .size:           2
        .value_kind:     hidden_remainder_y
      - .offset:         198
        .size:           2
        .value_kind:     hidden_remainder_z
      - .offset:         216
        .size:           8
        .value_kind:     hidden_global_offset_x
      - .offset:         224
        .size:           8
        .value_kind:     hidden_global_offset_y
      - .offset:         232
        .size:           8
        .value_kind:     hidden_global_offset_z
      - .offset:         240
        .size:           2
        .value_kind:     hidden_grid_dims
    .group_segment_fixed_size: 54528
    .kernarg_segment_align: 8
    .kernarg_segment_size: 432
    .language:       OpenCL C
    .language_version:
      - 2
      - 0
    .max_flat_workgroup_size: 512
    .name:           _Z8k_passCUILi1EEvPKiS1_PKfPKtS5_S3_S3_S3_S3_S3_S3_PK15HIP_vector_typeIjLj4EES9_S9_PKdSB_S1_S1_S5_S3_PtPd
    .private_segment_fixed_size: 0
    .sgpr_count:     35
    .sgpr_spill_count: 0
    .symbol:         _Z8k_passCUILi1EEvPKiS1_PKfPKtS5_S3_S3_S3_S3_S3_S3_PK15HIP_vector_typeIjLj4EES9_S9_PKdSB_S1_S1_S5_S3_PtPd.kd
    .uniform_work_group_size: 1
    .uses_dynamic_stack: false
    .vgpr_count:     126
    .vgpr_spill_count: 0
    .wavefront_size: 64
  - .agpr_count:     64
    .args:
      - .actual_access:  read_only
        .address_space:  global
        .offset:         0
        .size:           8
        .value_kind:     global_buffer
      - .address_space:  global
        .offset:         8
        .size:           8
        .value_kind:     global_buffer
      - .actual_access:  read_only
        .address_space:  global
        .offset:         16
        .size:           8
        .value_kind:     global_buffer
      - .actual_access:  read_only
        .address_space:  global
        .offset:         24
        .size:           8
        .value_kind:     global_buffer
      - .actual_access:  read_only
        .address_space:  global
        .offset:         32
        .size:           8
        .value_kind:     global_buffer
      - .actual_access:  read_only
        .address_space:  global
        .offset:         40
        .size:           8
        .value_kind:     global_buffer
      - .actual_access:  read_only
        .address_space:  global
        .offset:         48
        .size:           8
        .value_kind:     global_buffer
      - .actual_access:  write_only
        .address_space:  global
        .offset:         56
        .size:           8
        .value_kind:     global_buffer
      - .actual_access:  write_only
        .address_space:  global
        .offset:         64
        .size:           8
        .value_kind:     global_buffer
      - .actual_access:  read_only
        .address_space:  global
        .offset:         72
        .size:           8
        .value_kind:     global_buffer
      - .actual_access:  read_only
        .address_space:  global
        .offset:         80
        .size:           8
        .value_kind:     global_buffer
      - .offset:         88
        .size:           4
        .value_kind:     hidden_block_count_x
      - .offset:         92
        .size:           4
        .value_kind:     hidden_block_count_y
      - .offset:         96
        .size:           4
        .value_kind:     hidden_block_count_z
      - .offset:         100
        .size:           2
        .value_kind:     hidden_group_size_x
      - .offset:         102
        .size:           2
        .value_kind:     hidden_group_size_y
      - .offset:         104
        .size:           2
        .value_kind:     hidden_group_size_z
      - .offset:         106
        .size:           2
        .value_kind:     hidden_remainder_x
      - .offset:         108
        .size:           2
        .value_kind:     hidden_remainder_y
      - .offset:         110
        .size:           2
        .value_kind:     hidden_remainder_z
      - .offset:         128
        .size:           8
        .value_kind:     hidden_global_offset_x
      - .offset:         136
        .size:           8
        .value_kind:     hidden_global_offset_y
      - .offset:         144
        .size:           8
        .value_kind:     hidden_global_offset_z
      - .offset:         152
        .size:           2
        .value_kind:     hidden_grid_dims
    .group_segment_fixed_size: 33280
    .kernarg_segment_align: 8
    .kernarg_segment_size: 344
    .language:       OpenCL C
    .language_version:
      - 2
      - 0
    .max_flat_workgroup_size: 256
    .name:           _Z4k_U3ILb0EtEvPKtPtPKdPKfS6_PK15HIP_vector_typeIjLj4EES6_PT0_SC_S6_Pd
    .private_segment_fixed_size: 0
    .sgpr_count:     20
    .sgpr_spill_count: 0
    .symbol:         _Z4k_U3ILb0EtEvPKtPtPKdPKfS6_PK15HIP_vector_typeIjLj4EES6_PT0_SC_S6_Pd.kd
    .uniform_work_group_size: 1
    .uses_dynamic_stack: false
    .vgpr_count:     144
    .vgpr_spill_count: 0
    .wavefront_size: 64
  - .agpr_count:     0
    .args:
      - .actual_access:  read_only
        .address_space:  global
        .offset:         0
        .size:           8
        .value_kind:     global_buffer
      - .actual_access:  read_only
        .address_space:  global
        .offset:         8
        .size:           8
        .value_kind:     global_buffer
      - .actual_access:  read_only
        .address_space:  global
        .offset:         16
        .size:           8
        .value_kind:     global_buffer
      - .actual_access:  read_only
        .address_space:  global
        .offset:         24
        .size:           8
        .value_kind:     global_buffer
      - .actual_access:  read_only
        .address_space:  global
        .offset:         32
        .size:           8
        .value_kind:     global_buffer
      - .actual_access:  read_only
        .address_space:  global
        .offset:         40
        .size:           8
        .value_kind:     global_buffer
      - .actual_access:  read_only
        .address_space:  global
        .offset:         48
        .size:           8
        .value_kind:     global_buffer
      - .actual_access:  read_only
        .address_space:  global
        .offset:         56
        .size:           8
        .value_kind:     global_buffer
      - .actual_access:  read_only
        .address_space:  global
        .offset:         64
        .size:           8
        .value_kind:     global_buffer
      - .actual_access:  read_only
        .address_space:  global
        .offset:         72
        .size:           8
        .value_kind:     global_buffer
      - .address_space:  global
        .offset:         80
        .size:           8
        .value_kind:     global_buffer
      - .offset:         88
        .size:           4
        .value_kind:     hidden_block_count_x
      - .offset:         92
        .size:           4
        .value_kind:     hidden_block_count_y
      - .offset:         96
        .size:           4
        .value_kind:     hidden_block_count_z
      - .offset:         100
        .size:           2
        .value_kind:     hidden_group_size_x
      - .offset:         102
        .size:           2
        .value_kind:     hidden_group_size_y
      - .offset:         104
        .size:           2
        .value_kind:     hidden_group_size_z
      - .offset:         106
        .size:           2
        .value_kind:     hidden_remainder_x
      - .offset:         108
        .size:           2
        .value_kind:     hidden_remainder_y
      - .offset:         110
        .size:           2
        .value_kind:     hidden_remainder_z
      - .offset:         128
        .size:           8
        .value_kind:     hidden_global_offset_x
      - .offset:         136
        .size:           8
        .value_kind:     hidden_global_offset_y
      - .offset:         144
        .size:           8
        .value_kind:     hidden_global_offset_z
      - .offset:         152
        .size:           2
        .value_kind:     hidden_grid_dims
    .group_segment_fixed_size: 784
    .kernarg_segment_align: 8
    .kernarg_segment_size: 344
    .language:       OpenCL C
    .language_version:
      - 2
      - 0
    .max_flat_workgroup_size: 256
    .name:           _Z4k_U3ILb1EtEvPKtPtPKdPKfS6_PK15HIP_vector_typeIjLj4EES6_PT0_SC_S6_Pd
    .private_segment_fixed_size: 0
    .sgpr_count:     20
    .sgpr_spill_count: 0
    .symbol:         _Z4k_U3ILb1EtEvPKtPtPKdPKfS6_PK15HIP_vector_typeIjLj4EES6_PT0_SC_S6_Pd.kd
    .uniform_work_group_size: 1
    .uses_dynamic_stack: false
    .vgpr_count:     79
    .vgpr_spill_count: 0
    .wavefront_size: 64
